# P8 block-start LDS table fill: 20 loads into distinct registers issued before one wait (was ten load-pair/wait/LDS-write rounds)
# speedup vs baseline: 1.0019x; 1.0019x over previous
.LBB0_1027:
	v_add_u32_e32 v4, s28, v0
	v_add_u32_e32 v6, s28, v1
	v_ashrrev_i32_e32 v5, 31, v4
	v_ashrrev_i32_e32 v7, 31, v6
	v_lshl_add_u64 v[4:5], v[4:5], 2, s[14:15]
	v_lshl_add_u64 v[6:7], v[6:7], 2, s[14:15]
	global_load_dword v20, v[4:5], off
	global_load_dword v21, v[6:7], off
	v_ashrrev_i32_e32 v5, 31, v1
	v_mov_b32_e32 v4, v1
	v_ashrrev_i32_e32 v7, 31, v0
	v_mov_b32_e32 v6, v0
	v_lshlrev_b64 v[6:7], 2, v[6:7]
	v_lshlrev_b64 v[10:11], 2, v[4:5]
	v_lshl_add_u64 v[4:5], s[48:49], 0, v[10:11]
	v_add_u32_e32 v2, -2, v2
	s_add_i32 s29, s29, 4
	v_cmp_eq_u32_e32 vcc, 0, v2
	s_or_b64 s[24:25], vcc, s[24:25]
	v_lshl_add_u64 v[8:9], s[48:49], 0, v[6:7]
	global_load_dword v22, v[8:9], off
	s_nop 0
	global_load_dword v23, v[4:5], off
	v_lshl_add_u64 v[6:7], s[50:51], 0, v[6:7]
	v_add_u32_e32 v4, 0x2000, v3
	v_lshl_add_u64 v[8:9], s[50:51], 0, v[10:11]
	global_load_dword v24, v[6:7], off
	s_nop 0
	global_load_dword v25, v[8:9], off
	v_add_u32_e32 v8, s27, v0
	v_add_u32_e32 v10, s27, v1
	v_ashrrev_i32_e32 v9, 31, v8
	v_ashrrev_i32_e32 v11, 31, v10
	v_lshl_add_u64 v[8:9], v[8:9], 2, s[14:15]
	v_lshl_add_u64 v[10:11], v[10:11], 2, s[14:15]
	global_load_dword v26, v[8:9], off
	s_nop 0
	global_load_dword v27, v[10:11], off
	v_add_u32_e32 v6, s26, v0
	v_add_u32_e32 v8, s26, v1
	v_ashrrev_i32_e32 v7, 31, v6
	v_ashrrev_i32_e32 v9, 31, v8
	v_lshl_add_u64 v[6:7], v[6:7], 2, s[14:15]
	v_lshl_add_u64 v[8:9], v[8:9], 2, s[14:15]
	global_load_dword v28, v[6:7], off
	s_nop 0
	global_load_dword v29, v[8:9], off
	v_add_u32_e32 v8, 0x400, v0
	v_add_u32_e32 v10, s28, v8
	v_ashrrev_i32_e32 v11, 31, v10
	v_lshl_add_u64 v[10:11], v[10:11], 2, s[14:15]
	v_ashrrev_i32_e32 v9, 31, v8
	v_add_u32_e32 v0, 0x800, v0
	v_add_u32_e32 v6, 0x400, v1
	v_add_u32_e32 v12, s28, v6
	v_ashrrev_i32_e32 v13, 31, v12
	v_lshl_add_u64 v[12:13], v[12:13], 2, s[14:15]
	global_load_dword v30, v[10:11], off
	s_nop 0
	global_load_dword v31, v[12:13], off
	v_ashrrev_i32_e32 v7, 31, v6
	v_lshlrev_b64 v[14:15], 2, v[6:7]
	v_lshl_add_u64 v[16:17], s[48:49], 0, v[14:15]
	v_add_u32_e32 v1, 0x800, v1
	v_lshlrev_b64 v[10:11], 2, v[8:9]
	v_lshl_add_u64 v[12:13], s[48:49], 0, v[10:11]
	global_load_dword v32, v[12:13], off
	global_load_dword v33, v[16:17], off
	v_lshl_add_u64 v[10:11], s[50:51], 0, v[10:11]
	v_lshl_add_u64 v[12:13], s[50:51], 0, v[14:15]
	v_add_u32_e32 v14, s27, v6
	v_ashrrev_i32_e32 v15, 31, v14
	v_lshl_add_u64 v[14:15], v[14:15], 2, s[14:15]
	v_add_u32_e32 v6, s26, v6
	global_load_dword v34, v[10:11], off
	s_nop 0
	global_load_dword v35, v[12:13], off
	v_add_u32_e32 v12, s27, v8
	v_ashrrev_i32_e32 v13, 31, v12
	v_lshl_add_u64 v[12:13], v[12:13], 2, s[14:15]
	global_load_dword v36, v[12:13], off
	s_nop 0
	global_load_dword v37, v[14:15], off
	v_add_u32_e32 v8, s26, v8
	v_ashrrev_i32_e32 v7, 31, v6
	v_ashrrev_i32_e32 v9, 31, v8
	v_lshl_add_u64 v[8:9], v[8:9], 2, s[14:15]
	v_lshl_add_u64 v[6:7], v[6:7], 2, s[14:15]
	global_load_dword v38, v[8:9], off
	s_nop 0
	global_load_dword v39, v[6:7], off
	s_waitcnt vmcnt(0)
	ds_write2st64_b32 v3, v20, v21 offset1:8
	ds_write2st64_b32 v3, v22, v23 offset0:32 offset1:40
	v_pk_add_f32 v[26:27], v[26:27], 1.0 op_sel_hi:[1,0]
	s_nop 0
	v_pk_mul_f32 v[24:25], v[24:25], v[26:27]
	ds_write2st64_b32 v3, v24, v25 offset0:64 offset1:72
	ds_write2st64_b32 v3, v28, v29 offset0:128 offset1:136
	ds_write2st64_b32 v3, v30, v31 offset0:16 offset1:24
	ds_write2st64_b32 v3, v32, v33 offset0:48 offset1:56
	v_pk_add_f32 v[36:37], v[36:37], 1.0 op_sel_hi:[1,0]
	s_nop 0
	v_pk_mul_f32 v[34:35], v[34:35], v[36:37]
	ds_write2st64_b32 v3, v34, v35 offset0:80 offset1:88
	ds_write2st64_b32 v3, v38, v39 offset0:144 offset1:152
	v_mov_b32_e32 v5, s29
	v_mov_b32_e32 v3, v4
	s_andn2_b64 exec, exec, s[24:25]
	s_cbranch_execnz .LBB0_1027
	s_or_b64 exec, exec, s[24:25]
	v_lshlrev_b32_e32 v2, 9, v5
